# speedup vs baseline: 1.0390x; 1.0390x over previous
.LBB0_22:
	s_andn2_saveexec_b64 s[10:11], s[2:3]
	s_cbranch_execz .LBB0_40
	v_add_u32_e32 v2, 0xfffc81c0, v2
	v_lshrrev_b32_e32 v1, 7, v2
	v_mul_lo_u16_e32 v3, 0xab, v1
	v_lshrrev_b16_e32 v3, 9, v3
	s_load_dwordx2 s[2:3], s[0:1], 0x18
	v_mul_lo_u16_e32 v3, 3, v3
	v_sub_u16_e32 v1, v1, v3
	v_and_b32_e32 v4, 31, v0
	v_lshlrev_b16_e32 v1, 5, v1
	v_lshrrev_b32_e32 v5, 2, v2
	v_lshrrev_b32_e32 v0, 3, v0
	v_and_b32_e32 v1, 0xe0, v1
	v_and_b32_e32 v5, 16, v5
	v_and_b32_e32 v0, 4, v0
	v_or3_b32 v6, v5, v0, v1
	s_movk_i32 s12, 0x55
	v_mov_b32_e32 v1, 0
	v_lshlrev_b32_e32 v0, 2, v4
	v_mul_u32_u24_e32 v3, 0xaaab, v2
	v_cmp_gt_u32_e32 vcc, 10, v4
	s_waitcnt lgkmcnt(0)
	v_lshl_add_u64 v[4:5], s[2:3], 0, v[0:1]
	v_cmp_gt_u32_e64 s[2:3], s12, v6
	v_mul_lo_u16_sdwa v3, v3, s12 dst_sel:DWORD dst_unused:UNUSED_PAD src0_sel:BYTE_3 src1_sel:DWORD
	v_mov_b32_e32 v0, 0
	v_mov_b32_e32 v1, 0
	v_mov_b32_e32 v8, 0
	v_mov_b32_e32 v7, 0
	v_mov_b32_e32 v10, 0
	v_mov_b32_e32 v9, 0
	v_mov_b32_e32 v12, 0
	v_mov_b32_e32 v11, 0
	v_mov_b32_e32 v13, v6
	v_cmp_gt_u32_e64 s[2:3], s12, v13
	s_and_b64 s[14:15], vcc, s[2:3]
	s_and_saveexec_b64 s[2:3], s[14:15]
	v_add_u32_e32 v13, v13, v3
	v_mad_u64_u32 v[14:15], s[16:17], v13, 40, v[4:5]
	global_load_dword v0, v[14:15], off
	s_mov_b64 exec, s[2:3]
	v_or_b32_e32 v13, 1, v6
	v_cmp_gt_u32_e64 s[2:3], s12, v13
	s_and_b64 s[14:15], vcc, s[2:3]
	s_and_saveexec_b64 s[2:3], s[14:15]
	v_add_u32_e32 v13, v13, v3
	v_mad_u64_u32 v[14:15], s[16:17], v13, 40, v[4:5]
	global_load_dword v1, v[14:15], off
	s_mov_b64 exec, s[2:3]
	v_or_b32_e32 v13, 2, v6
	v_cmp_gt_u32_e64 s[2:3], s12, v13
	s_and_b64 s[14:15], vcc, s[2:3]
	s_and_saveexec_b64 s[2:3], s[14:15]
	v_add_u32_e32 v13, v13, v3
	v_mad_u64_u32 v[14:15], s[16:17], v13, 40, v[4:5]
	global_load_dword v8, v[14:15], off
	s_mov_b64 exec, s[2:3]
	v_or_b32_e32 v13, 3, v6
	v_cmp_gt_u32_e64 s[2:3], s12, v13
	s_and_b64 s[14:15], vcc, s[2:3]
	s_and_saveexec_b64 s[2:3], s[14:15]
	v_add_u32_e32 v13, v13, v3
	v_mad_u64_u32 v[14:15], s[16:17], v13, 40, v[4:5]
	global_load_dword v7, v[14:15], off
	s_mov_b64 exec, s[2:3]
	v_or_b32_e32 v13, 8, v6
	v_cmp_gt_u32_e64 s[2:3], s12, v13
	s_and_b64 s[14:15], vcc, s[2:3]
	s_and_saveexec_b64 s[2:3], s[14:15]
	v_add_u32_e32 v13, v13, v3
	v_mad_u64_u32 v[14:15], s[16:17], v13, 40, v[4:5]
	global_load_dword v10, v[14:15], off
	s_mov_b64 exec, s[2:3]
	v_or_b32_e32 v13, 9, v6
	v_cmp_gt_u32_e64 s[2:3], s12, v13
	s_and_b64 s[14:15], vcc, s[2:3]
	s_and_saveexec_b64 s[2:3], s[14:15]
	v_add_u32_e32 v13, v13, v3
	v_mad_u64_u32 v[14:15], s[16:17], v13, 40, v[4:5]
	global_load_dword v9, v[14:15], off
	s_mov_b64 exec, s[2:3]
	v_or_b32_e32 v13, 10, v6
	v_cmp_gt_u32_e64 s[2:3], s12, v13
	s_and_b64 s[14:15], vcc, s[2:3]
	s_and_saveexec_b64 s[2:3], s[14:15]
	v_add_u32_e32 v13, v13, v3
	v_mad_u64_u32 v[14:15], s[16:17], v13, 40, v[4:5]
	global_load_dword v12, v[14:15], off
	s_mov_b64 exec, s[2:3]
	v_or_b32_e32 v13, 11, v6
	v_cmp_gt_u32_e64 s[2:3], s12, v13
	s_and_b64 s[14:15], vcc, s[2:3]
	s_and_saveexec_b64 s[2:3], s[14:15]
	v_add_u32_e32 v13, v13, v3
	v_mad_u64_u32 v[14:15], s[16:17], v13, 40, v[4:5]
	global_load_dword v11, v[14:15], off
	s_mov_b64 exec, s[2:3]
	s_waitcnt vmcnt(0)
	v_cvt_f16_f32_e32 v0, v0
	v_cvt_f16_f32_e32 v1, v1
	v_cvt_f16_f32_e32 v8, v8
	v_cvt_f16_f32_e32 v7, v7
	v_cvt_f16_f32_e32 v10, v10
	v_cvt_f16_f32_e32 v9, v9
	v_cvt_f16_f32_e32 v12, v12
	v_cvt_f16_f32_e32 v11, v11

.LBB0_41:
	s_andn2_saveexec_b64 s[2:3], s[8:9]
	s_cbranch_execz .LBB0_59
	s_load_dwordx2 s[8:9], s[0:1], 0x0
	v_add_u32_e32 v2, 0xfffc8e00, v2
	v_and_b32_e32 v4, 31, v0
	v_lshrrev_b32_e32 v0, 3, v0
	v_and_b32_e32 v0, 4, v0
	v_lshrrev_b32_e32 v1, 2, v2
	s_mov_b32 s10, 0x3ffffff0
	v_cmp_gt_u32_e32 vcc, 24, v4
	v_and_or_b32 v6, v1, s10, v0
	v_mov_b32_e32 v1, 0
	v_mov_b32_e32 v0, 0
	v_mov_b32_e32 v5, 0
	v_mov_b32_e32 v3, 0
	v_mov_b32_e32 v8, 0
	v_mov_b32_e32 v7, 0
	v_mov_b32_e32 v10, 0
	v_mov_b32_e32 v9, 0
	s_and_saveexec_b64 s[10:11], vcc
	v_mul_lo_u32 v11, v6, 24
	v_or_b32_e32 v12, v11, v4
	v_mov_b32_e32 v13, 0
	s_waitcnt lgkmcnt(0)
	v_lshl_add_u64 v[12:13], v[12:13], 2, s[8:9]
	global_load_dword v1, v[12:13], off
	global_load_dword v0, v[12:13], off offset:96
	global_load_dword v5, v[12:13], off offset:192
	global_load_dword v3, v[12:13], off offset:288
	global_load_dword v8, v[12:13], off offset:768
	global_load_dword v7, v[12:13], off offset:864
	global_load_dword v10, v[12:13], off offset:960
	global_load_dword v9, v[12:13], off offset:1056
	s_waitcnt vmcnt(0)
	v_mul_f32_e32 v1, 0x44800000, v1
	v_mul_f32_e32 v0, 0x44800000, v0
	v_mul_f32_e32 v5, 0x44800000, v5
	v_mul_f32_e32 v3, 0x44800000, v3
	v_mul_f32_e32 v8, 0x44800000, v8
	v_mul_f32_e32 v7, 0x44800000, v7
	v_mul_f32_e32 v10, 0x44800000, v10
	v_mul_f32_e32 v9, 0x44800000, v9

.LBB0_60:
	v_ashrrev_i32_e32 v1, 6, v2
	s_mov_b32 s2, 0x55555556
	v_mul_hi_i32 v3, v1, s2
	v_lshrrev_b32_e32 v4, 31, v3
	v_add_u32_e32 v3, v3, v4
	s_mov_b32 s2, 0x5397829d
	v_mul_hi_i32 v5, v3, s2
	v_lshrrev_b32_e32 v6, 31, v5
	v_lshrrev_b32_e32 v5, 4, v5
	v_lshl_add_u32 v4, v3, 1, v3
	v_add_u32_e32 v5, v5, v6
	s_mov_b32 s2, 0x6f74ae27
	s_load_dwordx2 s[0:1], s[0:1], 0x8
	v_sub_u32_e32 v4, v1, v4
	v_mul_lo_u32 v5, v5, 49
	v_mul_hi_i32 v1, v1, s2
	v_sub_u32_e32 v3, v3, v5
	v_lshrrev_b32_e32 v5, 31, v1
	v_lshrrev_b32_e32 v1, 6, v1
	v_add_u32_e32 v1, v1, v5
	v_and_b32_e32 v5, 31, v0
	v_lshl_or_b32 v6, v4, 5, v5
	v_lshrrev_b32_e32 v0, 2, v0
	v_mul_i32_i24_e32 v1, 0x310, v1
	s_movk_i32 s2, 0x55
	v_and_or_b32 v0, v0, 8, v1
	v_ashrrev_i32_e32 v7, 31, v6
	v_cmp_gt_i32_e32 vcc, s2, v6
	v_lshl_add_u32 v5, v3, 4, v0
	s_waitcnt lgkmcnt(0)
	v_lshl_add_u64 v[0:1], v[6:7], 2, s[0:1]
	v_mov_b32_e32 v3, 0
	v_mov_b32_e32 v4, 0
	v_mov_b32_e32 v7, 0
	v_mov_b32_e32 v6, 0
	v_mov_b32_e32 v9, 0
	v_mov_b32_e32 v8, 0
	v_mov_b32_e32 v11, 0
	v_mov_b32_e32 v10, 0
	s_and_saveexec_b64 s[0:1], vcc
	s_movk_i32 s2, 0x154
	v_mad_i64_i32 v[12:13], s[2:3], v5, s2, v[0:1]
	global_load_dword v3, v[12:13], off
	global_load_dword v4, v[12:13], off offset:340
	global_load_dword v7, v[12:13], off offset:680
	global_load_dword v6, v[12:13], off offset:1020
	global_load_dword v9, v[12:13], off offset:1360
	global_load_dword v8, v[12:13], off offset:1700
	global_load_dword v11, v[12:13], off offset:2040
	global_load_dword v10, v[12:13], off offset:2380
	s_waitcnt vmcnt(0)
	v_cvt_f16_f32_e32 v3, v3
	v_cvt_f16_f32_e32 v4, v4
	v_cvt_f16_f32_e32 v7, v7
	v_cvt_f16_f32_e32 v6, v6
	v_cvt_f16_f32_e32 v9, v9
	v_cvt_f16_f32_e32 v8, v8
	v_cvt_f16_f32_e32 v11, v11
	v_cvt_f16_f32_e32 v10, v10
